# grid barrier: workgroups that are not last in their XCD wait on the global generation word directly instead of the per-XCD generation word (one release hop less)
# speedup vs baseline: 1.0248x; 1.0066x over previous
.LBB0_66:
	v_readlane_b32 s0, v254, 6
	s_lshl_b32 s0, s0, 8
	v_readlane_b32 s2, v254, 4
	v_readlane_b32 s3, v254, 5
	s_add_u32 s6, s2, s0
	s_addc_u32 s7, s3, 0
	v_mov_b32_e32 v1, 0x1000
	v_mov_b32_e32 v3, 1
	global_atomic_add v3, v1, v3, s[6:7] offset:1024 sc0
	v_cvt_f32_u32_e32 v1, v2
	v_sub_u32_e32 v4, 0, v2
	v_rcp_iflag_f32_e32 v1, v1
	s_nop 0
	v_mul_f32_e32 v1, 0x4f7ffffe, v1
	v_cvt_u32_f32_e32 v1, v1
	v_mul_lo_u32 v4, v4, v1
	v_mul_hi_u32 v4, v1, v4
	v_add_u32_e32 v1, v1, v4
	s_waitcnt vmcnt(0)
	v_mul_hi_u32 v1, v3, v1
	v_mul_lo_u32 v4, v1, v2
	v_sub_u32_e32 v4, v3, v4
	v_add_u32_e32 v5, 1, v1
	v_cmp_ge_u32_e32 vcc, v4, v2
	v_add_u32_e32 v3, 1, v3
	s_nop 0
	v_cndmask_b32_e32 v1, v1, v5, vcc
	v_sub_u32_e32 v5, v4, v2
	v_cndmask_b32_e32 v4, v4, v5, vcc
	v_add_u32_e32 v5, 1, v1
	v_cmp_ge_u32_e32 vcc, v4, v2
	s_nop 1
	v_cndmask_b32_e32 v1, v1, v5, vcc
	v_mul_lo_u32 v4, v2, v1
	v_add_u32_e32 v2, v4, v2
	v_cmp_ne_u32_e32 vcc, v3, v2
	s_and_saveexec_b64 s[0:1], vcc
	s_xor_b64 s[8:9], exec, s[0:1]
	s_cbranch_execz .LBB0_80
	s_waitcnt lgkmcnt(0)
	s_add_u32 s14, s26, 0x7500
	s_addc_u32 s15, s27, 0
	v_mov_b32_e32 v0, 0
	global_load_dword v0, v0, s[14:15] sc1
	s_waitcnt vmcnt(0)
	v_cmp_eq_u32_e32 vcc, v0, v1
	s_and_saveexec_b64 s[10:11], vcc
	s_cbranch_execz .LBB0_79
	s_add_u32 s12, s26, 0x4200
	s_addc_u32 s13, s27, 0
	s_mov_b32 s0, 1
	s_mov_b64 s[16:17], 0
	v_mov_b32_e32 v0, 0
	s_branch .LBB0_70
